# phase 3 tail (in-proj weight rows -> int8): next row's loads issued while the current row is reduced/converted (second register set)
# speedup vs baseline: 1.0068x; 1.0021x over previous
; __device__ __forceinline__ void quant_weight_rows_i8(const bf16_t* __restrict__ src, int8_t* __restrict__ dst, float* __restrict__ scl,
;                                                      int nrows, int bid, int nb) {
;   const int lane = threadIdx.x & 63, w = threadIdx.x >> 6;
;   for (int n = bid * 4 + w; n < nrows; n += nb * 4) {
;     const bf16_t* wr = src + (size_t)n * D;
;     uint4 q[4];
; #pragma unroll
;     for (int c = 0; c < 4; ++c) q[c] = *reinterpret_cast<const uint4*>(wr + c * 512 + lane * 8);
.LBB0_174:
	s_or_b64 exec, exec, s[10:11]
	s_movk_i32 s3, 0x1280
	v_cmp_gt_i32_e32 vcc, s3, v186
	s_and_saveexec_b64 s[10:11], vcc
	s_cbranch_execz .LBB0_179
	v_mbcnt_hi_u32_b32 v2, -1, v191
	v_and_b32_e32 v4, 64, v2
	v_xor_b32_e32 v3, 16, v2
	v_add_u32_e32 v4, 64, v4
	v_cmp_lt_i32_e32 vcc, v3, v4
	s_load_dwordx2 s[14:15], s[8:9], 0x148
	s_load_dwordx2 s[16:17], s[8:9], 0x100
	s_load_dwordx2 s[12:13], s[8:9], 0x110
	v_cndmask_b32_e32 v3, v2, v3, vcc
	v_lshlrev_b32_e32 v8, 2, v3
	v_xor_b32_e32 v3, 32, v2
	v_cmp_lt_i32_e32 vcc, v3, v4
	v_lshlrev_b64 v[4:5], 12, v[186:187]
	v_lshlrev_b64 v[6:7], 11, v[186:187]
	s_lshl_b32 s8, s34, 2
	v_lshl_or_b32 v4, v184, 4, v4
	v_lshl_or_b32 v6, v184, 3, v6
	v_cndmask_b32_e32 v2, v2, v3, vcc
	s_ashr_i32 s9, s8, 31
	s_waitcnt lgkmcnt(0)
	v_lshl_add_u64 v[4:5], s[14:15], 0, v[4:5]
	s_mov_b64 s[14:15], 0xc0c
	v_lshl_add_u64 v[6:7], s[16:17], 0, v[6:7]
	s_mov_b64 s[16:17], 0x400
	v_lshlrev_b32_e32 v9, 2, v2
	v_cmp_eq_u32_e64 s[6:7], 0, v184
	v_lshl_add_u64 v[2:3], v[186:187], 2, s[12:13]
	s_lshl_b64 s[12:13], s[8:9], 2
	v_lshl_add_u64 v[4:5], v[4:5], 0, s[14:15]
	s_lshl_b64 s[14:15], s[8:9], 12
	v_lshl_add_u64 v[6:7], v[6:7], 0, s[16:17]
	s_lshl_b64 s[16:17], s[8:9], 11
	s_mov_b64 s[18:19], 0
	s_mov_b32 s3, 0x42fe0000
	s_movk_i32 s9, 0x127f
	v_mov_b32_e32 v10, v186
	global_load_dwordx4 v[200:203], v[4:5], off offset:-3084
	global_load_dwordx4 v[204:207], v[4:5], off offset:-2060
	global_load_dwordx4 v[208:211], v[4:5], off offset:-1036
	global_load_dwordx4 v[212:215], v[4:5], off offset:-12
	s_waitcnt vmcnt(0)
	s_branch .Lmy_q3_in

; __device__ __forceinline__ float bflo(uint32_t w) { return __uint_as_float(w << 16); }
; __device__ __forceinline__ float bfhi(uint32_t w) { return __uint_as_float(w & 0xffff0000u); }
; __device__ __forceinline__ void quant_weight_rows_i8(const bf16_t* __restrict__ src, int8_t* __restrict__ dst, float* __restrict__ scl,
;                                                      int nrows, int bid, int nb) {
;     ...
;   for (int n = bid * 4 + w; n < nrows; n += nb * 4) {
;     const bf16_t* wr = src + (size_t)n * D;
;     uint4 q[4];
; #pragma unroll
;     for (int c = 0; c < 4; ++c) q[c] = *reinterpret_cast<const uint4*>(wr + c * 512 + lane * 8);
;     float am = 0.f;
; #pragma unroll
;     for (int c = 0; c < 4; ++c) {
;       am = fmaxf(am, fmaxf(fmaxf(fabsf(bflo(q[c].x)), fabsf(bfhi(q[c].x))), fmaxf(fabsf(bflo(q[c].y)), fabsf(bfhi(q[c].y)))));
;       am = fmaxf(am, fmaxf(fmaxf(fabsf(bflo(q[c].z)), fabsf(bfhi(q[c].z))), fmaxf(fabsf(bflo(q[c].w)), fabsf(bfhi(q[c].w)))));
;     }
;     am = wave_max_fast(am);
.LBB0_177:
	s_waitcnt vmcnt(4)
.Lmy_q3_in:
	v_mov_b32_e32 v12, v200
	v_mov_b32_e32 v13, v201
	v_mov_b32_e32 v14, v202
	v_mov_b32_e32 v15, v203
	v_mov_b32_e32 v16, v204
	v_mov_b32_e32 v17, v205
	v_mov_b32_e32 v18, v206
	v_mov_b32_e32 v19, v207
	v_mov_b32_e32 v20, v208
	v_mov_b32_e32 v21, v209
	v_mov_b32_e32 v22, v210
	v_mov_b32_e32 v23, v211
	v_mov_b32_e32 v24, v212
	v_mov_b32_e32 v25, v213
	v_mov_b32_e32 v26, v214
	v_mov_b32_e32 v27, v215
	v_lshl_add_u64 v[216:217], v[4:5], 0, s[14:15]
	global_load_dwordx4 v[200:203], v[216:217], off offset:-3084
	global_load_dwordx4 v[204:207], v[216:217], off offset:-2060
	global_load_dwordx4 v[208:211], v[216:217], off offset:-1036
	global_load_dwordx4 v[212:215], v[216:217], off offset:-12
	v_lshlrev_b32_e32 v29, 16, v13
	v_and_b32_e32 v13, 0xffff0000, v13
	v_lshlrev_b32_e32 v31, 16, v15
	v_and_b32_e32 v15, 0xffff0000, v15
	v_lshlrev_b32_e32 v33, 16, v17
	v_and_b32_e32 v17, 0xffff0000, v17
	v_lshlrev_b32_e32 v35, 16, v19
	v_and_b32_e32 v19, 0xffff0000, v19
	v_max_f32_e64 v11, |v13|, |v13|
	v_max_f32_e64 v44, |v29|, |v29|
	v_max_f32_e64 v45, |v15|, |v15|
	v_max_f32_e64 v46, |v31|, |v31|
	v_lshlrev_b32_e32 v28, 16, v12
	v_and_b32_e32 v12, 0xffff0000, v12
	v_lshlrev_b32_e32 v30, 16, v14
	v_and_b32_e32 v14, 0xffff0000, v14
	v_lshlrev_b32_e32 v37, 16, v21
	v_and_b32_e32 v21, 0xffff0000, v21
	v_lshlrev_b32_e32 v39, 16, v23
	v_and_b32_e32 v23, 0xffff0000, v23
	v_max_f32_e64 v47, |v17|, |v17|
	v_max_f32_e64 v48, |v33|, |v33|
	v_max_f32_e64 v49, |v19|, |v19|
	v_max_f32_e64 v50, |v35|, |v35|
	v_max_f32_e32 v11, v44, v11
	v_max_f32_e32 v44, v46, v45
	v_lshlrev_b32_e32 v32, 16, v16
	v_and_b32_e32 v16, 0xffff0000, v16
	v_lshlrev_b32_e32 v34, 16, v18
	v_and_b32_e32 v18, 0xffff0000, v18
	v_lshlrev_b32_e32 v41, 16, v25
	v_and_b32_e32 v25, 0xffff0000, v25
	v_lshlrev_b32_e32 v43, 16, v27
	v_and_b32_e32 v27, 0xffff0000, v27
	v_max_f32_e64 v51, |v21|, |v21|
	v_max_f32_e64 v52, |v37|, |v37|
	v_max_f32_e64 v53, |v23|, |v23|
	v_max_f32_e64 v54, |v39|, |v39|
	v_max_f32_e32 v45, v48, v47
	v_max_f32_e32 v46, v50, v49
	v_max3_f32 v11, |v28|, |v12|, v11
	v_max3_f32 v44, |v30|, |v14|, v44
	v_lshlrev_b32_e32 v36, 16, v20
	v_and_b32_e32 v20, 0xffff0000, v20
	v_lshlrev_b32_e32 v38, 16, v22
	v_and_b32_e32 v22, 0xffff0000, v22
	v_max_f32_e64 v55, |v25|, |v25|
	v_max_f32_e64 v56, |v41|, |v41|
	v_max_f32_e64 v57, |v27|, |v27|
	v_max_f32_e64 v58, |v43|, |v43|
	v_max_f32_e32 v47, v52, v51
	v_max_f32_e32 v48, v54, v53
	v_max3_f32 v45, |v32|, |v16|, v45
	v_max3_f32 v46, |v34|, |v18|, v46
	v_max3_f32 v11, v11, 0, v44
	v_lshlrev_b32_e32 v40, 16, v24
	v_and_b32_e32 v24, 0xffff0000, v24
	v_lshlrev_b32_e32 v42, 16, v26
	v_and_b32_e32 v26, 0xffff0000, v26
	v_max_f32_e32 v49, v56, v55
	v_max_f32_e32 v50, v58, v57
	v_max3_f32 v47, |v36|, |v20|, v47
	v_max3_f32 v48, |v38|, |v22|, v48
	v_max3_f32 v11, v11, v45, v46
	v_max3_f32 v49, |v40|, |v24|, v49
	v_max3_f32 v50, |v42|, |v26|, v50
	v_max3_f32 v11, v11, v47, v48
	v_max3_f32 v11, v11, v49, v50
	s_nop 1
	v_mov_b32_dpp v44, v11 quad_perm:[1,0,3,2] row_mask:0xf bank_mask:0xf bound_ctrl:1
	v_max_f32_e32 v44, v44, v44
	v_max_f32_e32 v11, v11, v44
	s_nop 1
	v_mov_b32_dpp v44, v11 quad_perm:[2,3,0,1] row_mask:0xf bank_mask:0xf bound_ctrl:1
	v_max_f32_e32 v44, v44, v44
	v_max_f32_e32 v11, v11, v44
	s_nop 1
	v_mov_b32_dpp v44, v11 row_ror:4 row_mask:0xf bank_mask:0xf bound_ctrl:1
	v_max_f32_e32 v44, v44, v44
	v_max_f32_e32 v11, v11, v44
	s_nop 1
	v_mov_b32_dpp v44, v11 row_ror:8 row_mask:0xf bank_mask:0xf bound_ctrl:1
	v_max_f32_e32 v44, v44, v44
	v_max_f32_e32 v11, v11, v44
	ds_bpermute_b32 v44, v8, v11
	s_waitcnt lgkmcnt(0)
	v_max_f32_e32 v44, v44, v44
	v_max_f32_e32 v11, v11, v44
	ds_bpermute_b32 v44, v9, v11
	s_waitcnt lgkmcnt(0)
; __device__ __forceinline__ float bflo(uint32_t w) { return __uint_as_float(w << 16); }
; __device__ __forceinline__ float bfhi(uint32_t w) { return __uint_as_float(w & 0xffff0000u); }
; __device__ __forceinline__ void quant_weight_rows_i8(const bf16_t* __restrict__ src, int8_t* __restrict__ dst, float* __restrict__ scl,
;                                                      int nrows, int bid, int nb) {
;     ...
;     am = wave_max_fast(am);
;     const float inv = (am > 0.f) ? 127.f / am : 0.f;
; #pragma unroll
;     for (int c = 0; c < 4; ++c) {
;       uint2 o;
;       o.x = pack_i8x4(bflo(q[c].x) * inv, bfhi(q[c].x) * inv, bflo(q[c].y) * inv, bfhi(q[c].y) * inv);
;       o.y = pack_i8x4(bflo(q[c].z) * inv, bfhi(q[c].z) * inv, bflo(q[c].w) * inv, bfhi(q[c].w) * inv);
;       *reinterpret_cast<uint2*>(dst + (size_t)n * D + c * 512 + lane * 8) = o;
;     }
;     if (lane == 0) scl[n] = am * (1.f / 127.f);
	v_max_f32_e32 v44, v44, v44
	v_max_f32_e32 v11, v11, v44
	v_div_scale_f32 v44, s[20:21], v11, v11, s3
	v_rcp_f32_e32 v45, v44
	v_div_scale_f32 v46, vcc, s3, v11, s3
	v_fma_f32 v47, -v44, v45, 1.0
	v_fmac_f32_e32 v45, v47, v45
	v_mul_f32_e32 v47, v46, v45
	v_fma_f32 v48, -v44, v47, v46
	v_fmac_f32_e32 v47, v48, v45
	v_fma_f32 v44, -v44, v47, v46
	v_div_fmas_f32 v44, v44, v45, v47
	v_div_fixup_f32 v44, v44, v11, s3
	v_cmp_lt_f32_e32 vcc, 0, v11
	s_nop 1
	v_cndmask_b32_e32 v44, 0, v44, vcc
	v_mul_f32_e32 v12, v44, v12
	v_mul_f32_e32 v14, v44, v14
	v_rndne_f32_e32 v12, v12
	v_rndne_f32_e32 v14, v14
	v_mul_f32_e32 v28, v44, v28
	v_mul_f32_e32 v30, v44, v30
	v_cvt_i32_f32_e32 v12, v12
	v_cvt_i32_f32_e32 v14, v14
	v_mul_f32_e32 v29, v44, v29
	v_mul_f32_e32 v13, v44, v13
	v_mul_f32_e32 v31, v44, v31
	v_mul_f32_e32 v15, v44, v15
	v_rndne_f32_e32 v28, v28
	v_rndne_f32_e32 v30, v30
	v_rndne_f32_e32 v29, v29
	v_rndne_f32_e32 v13, v13
	v_rndne_f32_e32 v31, v31
	v_rndne_f32_e32 v15, v15
	v_cvt_i32_f32_e32 v30, v30
	v_cvt_i32_f32_e32 v28, v28
	v_cvt_i32_f32_sdwa v29, v29 dst_sel:WORD_1 dst_unused:UNUSED_PAD src0_sel:DWORD
	v_cvt_i32_f32_sdwa v31, v31 dst_sel:WORD_1 dst_unused:UNUSED_PAD src0_sel:DWORD
	v_cvt_i32_f32_sdwa v13, v13 dst_sel:BYTE_3 dst_unused:UNUSED_PAD src0_sel:DWORD
	v_cvt_i32_f32_sdwa v15, v15 dst_sel:BYTE_3 dst_unused:UNUSED_PAD src0_sel:DWORD
	v_lshlrev_b32_e32 v14, 8, v14
	v_lshlrev_b32_e32 v12, 8, v12
	v_and_b32_e32 v14, 0xff00, v14
	v_and_b32_e32 v12, 0xff00, v12
	v_or_b32_sdwa v14, v30, v14 dst_sel:DWORD dst_unused:UNUSED_PAD src0_sel:BYTE_0 src1_sel:DWORD
	v_or_b32_sdwa v12, v28, v12 dst_sel:DWORD dst_unused:UNUSED_PAD src0_sel:BYTE_0 src1_sel:DWORD
	v_and_b32_e32 v31, 0xff0000, v31
	v_and_b32_e32 v29, 0xff0000, v29
	v_or_b32_e32 v14, v14, v15
	v_or_b32_e32 v12, v12, v13
	v_or_b32_e32 v13, v14, v31
	v_or_b32_e32 v12, v12, v29
	global_store_dwordx2 v[6:7], v[12:13], off offset:-1024
	v_mul_f32_e32 v13, v44, v16
	v_mul_f32_e32 v15, v44, v17
	v_mul_f32_e32 v17, v44, v18
	v_rndne_f32_e32 v13, v13
	v_rndne_f32_e32 v17, v17
	v_mul_f32_e32 v12, v44, v32
	v_mul_f32_e32 v16, v44, v34
	v_cvt_i32_f32_e32 v13, v13
	v_cvt_i32_f32_e32 v17, v17
	v_mul_f32_e32 v14, v44, v33
	v_rndne_f32_e32 v12, v12
	v_mul_f32_e32 v18, v44, v35
	v_mul_f32_e32 v19, v44, v19
	v_rndne_f32_e32 v16, v16
	v_rndne_f32_e32 v14, v14
	v_rndne_f32_e32 v15, v15
	v_rndne_f32_e32 v18, v18
	v_rndne_f32_e32 v19, v19
	v_cvt_i32_f32_e32 v16, v16
	v_cvt_i32_f32_e32 v12, v12
	v_cvt_i32_f32_sdwa v14, v14 dst_sel:WORD_1 dst_unused:UNUSED_PAD src0_sel:DWORD
	v_cvt_i32_f32_sdwa v18, v18 dst_sel:WORD_1 dst_unused:UNUSED_PAD src0_sel:DWORD
	v_cvt_i32_f32_sdwa v15, v15 dst_sel:BYTE_3 dst_unused:UNUSED_PAD src0_sel:DWORD
	v_cvt_i32_f32_sdwa v19, v19 dst_sel:BYTE_3 dst_unused:UNUSED_PAD src0_sel:DWORD
	v_lshlrev_b32_e32 v17, 8, v17
	v_lshlrev_b32_e32 v13, 8, v13
	v_and_b32_e32 v17, 0xff00, v17
	v_and_b32_e32 v13, 0xff00, v13
	v_or_b32_sdwa v16, v16, v17 dst_sel:DWORD dst_unused:UNUSED_PAD src0_sel:BYTE_0 src1_sel:DWORD
	v_or_b32_sdwa v12, v12, v13 dst_sel:DWORD dst_unused:UNUSED_PAD src0_sel:BYTE_0 src1_sel:DWORD
	v_and_b32_e32 v18, 0xff0000, v18
	v_and_b32_e32 v14, 0xff0000, v14
	v_or_b32_e32 v13, v16, v19
	v_or_b32_e32 v12, v12, v15
	v_or_b32_e32 v13, v13, v18
	v_or_b32_e32 v12, v12, v14
	global_store_dwordx2 v[6:7], v[12:13], off offset:-512
	v_mul_f32_e32 v13, v44, v20
	v_mul_f32_e32 v17, v44, v22
	v_rndne_f32_e32 v13, v13
	v_rndne_f32_e32 v17, v17
	v_mul_f32_e32 v12, v44, v36
	v_mul_f32_e32 v16, v44, v38
	v_cvt_i32_f32_e32 v13, v13
	v_cvt_i32_f32_e32 v17, v17
	v_mul_f32_e32 v14, v44, v37
	v_mul_f32_e32 v15, v44, v21
	v_rndne_f32_e32 v12, v12
	v_mul_f32_e32 v18, v44, v39
	v_mul_f32_e32 v19, v44, v23
	v_rndne_f32_e32 v16, v16
	v_rndne_f32_e32 v14, v14
	v_rndne_f32_e32 v15, v15
	v_rndne_f32_e32 v18, v18
	v_rndne_f32_e32 v19, v19
	v_cvt_i32_f32_e32 v16, v16
	v_cvt_i32_f32_e32 v12, v12
	v_cvt_i32_f32_sdwa v14, v14 dst_sel:WORD_1 dst_unused:UNUSED_PAD src0_sel:DWORD
	v_cvt_i32_f32_sdwa v18, v18 dst_sel:WORD_1 dst_unused:UNUSED_PAD src0_sel:DWORD
	v_cvt_i32_f32_sdwa v15, v15 dst_sel:BYTE_3 dst_unused:UNUSED_PAD src0_sel:DWORD
	v_cvt_i32_f32_sdwa v19, v19 dst_sel:BYTE_3 dst_unused:UNUSED_PAD src0_sel:DWORD
	v_lshlrev_b32_e32 v17, 8, v17
	v_lshlrev_b32_e32 v13, 8, v13
	v_and_b32_e32 v17, 0xff00, v17
	v_and_b32_e32 v13, 0xff00, v13
	v_or_b32_sdwa v16, v16, v17 dst_sel:DWORD dst_unused:UNUSED_PAD src0_sel:BYTE_0 src1_sel:DWORD
	v_or_b32_sdwa v12, v12, v13 dst_sel:DWORD dst_unused:UNUSED_PAD src0_sel:BYTE_0 src1_sel:DWORD
	v_and_b32_e32 v18, 0xff0000, v18
	v_and_b32_e32 v14, 0xff0000, v14
	v_or_b32_e32 v13, v16, v19
	v_or_b32_e32 v12, v12, v15
	v_or_b32_e32 v13, v13, v18
	v_or_b32_e32 v12, v12, v14
	global_store_dwordx2 v[6:7], v[12:13], off
	v_mul_f32_e32 v13, v44, v24
	v_mul_f32_e32 v17, v44, v26
	v_rndne_f32_e32 v13, v13
	v_rndne_f32_e32 v17, v17
	v_mul_f32_e32 v12, v44, v40
	v_mul_f32_e32 v16, v44, v42
	v_cvt_i32_f32_e32 v13, v13
	v_cvt_i32_f32_e32 v17, v17
	v_mul_f32_e32 v14, v44, v41
	v_mul_f32_e32 v15, v44, v25
	v_rndne_f32_e32 v12, v12
	v_mul_f32_e32 v18, v44, v43
	v_mul_f32_e32 v19, v44, v27
	v_rndne_f32_e32 v16, v16
	v_rndne_f32_e32 v14, v14
	v_rndne_f32_e32 v15, v15
	v_rndne_f32_e32 v18, v18
	v_rndne_f32_e32 v19, v19
	v_cvt_i32_f32_e32 v16, v16
	v_cvt_i32_f32_e32 v12, v12
	v_cvt_i32_f32_sdwa v14, v14 dst_sel:WORD_1 dst_unused:UNUSED_PAD src0_sel:DWORD
	v_cvt_i32_f32_sdwa v18, v18 dst_sel:WORD_1 dst_unused:UNUSED_PAD src0_sel:DWORD
	v_cvt_i32_f32_sdwa v15, v15 dst_sel:BYTE_3 dst_unused:UNUSED_PAD src0_sel:DWORD
	v_cvt_i32_f32_sdwa v19, v19 dst_sel:BYTE_3 dst_unused:UNUSED_PAD src0_sel:DWORD
	v_lshlrev_b32_e32 v17, 8, v17
	v_lshlrev_b32_e32 v13, 8, v13
	v_and_b32_e32 v17, 0xff00, v17
	v_and_b32_e32 v13, 0xff00, v13
	v_or_b32_sdwa v16, v16, v17 dst_sel:DWORD dst_unused:UNUSED_PAD src0_sel:BYTE_0 src1_sel:DWORD
	v_or_b32_sdwa v12, v12, v13 dst_sel:DWORD dst_unused:UNUSED_PAD src0_sel:BYTE_0 src1_sel:DWORD
	v_and_b32_e32 v18, 0xff0000, v18
	v_and_b32_e32 v14, 0xff0000, v14
	v_or_b32_e32 v13, v16, v19
	v_or_b32_e32 v12, v12, v15
	v_or_b32_e32 v13, v13, v18
	v_or_b32_e32 v12, v12, v14
	global_store_dwordx2 v[6:7], v[12:13], off offset:512
	s_and_saveexec_b64 s[20:21], s[6:7]
	s_cbranch_execz .LBB0_176
	v_mul_f32_e32 v11, 0x3c010204, v11
	global_store_dword v[2:3], v11, off
	s_branch .LBB0_176
